# s16p + one static s_setprio 1 for waves 4-7 before the attention block loop, reset after it (L0 and L1); padded
# speedup vs baseline: 1.0066x; 1.0066x over previous
; DI unsigned pk2(float lo, float hi) { const f32x2 v = {lo, hi}; return __builtin_bit_cast(unsigned, __builtin_convertvector(v, bf16x2_t)); }
; DI void attn_block(const Params& P, const Frame& F, int L, int b, int h, int qb, float lam, float oml) {
;     ...
;     const int lane = F.lane, c = lane & 15, rq = lane >> 4, wave = F.wave;
;     const int q0 = qb * 128, qrow = q0 + 16 * wave + c;
;     const size_t rowbase = (size_t)b * SEQ;
;     bf16x8 qf[2][2];
; #pragma unroll
;     for (int j = 0; j < 2; ++j)
; #pragma unroll
;         for (int ks = 0; ks < 2; ++ks) qf[j][ks] = *(const bf16x8*)(Z + (rowbase + qrow) * NZ + 3072 + h * 128 + j * 64 + 32 * ks + 8 * rq);
;     const float LOG2E = 1.4426950408889634f;
;     const float sc = 0.125f * LOG2E, sl = __builtin_bit_cast(float, __builtin_amdgcn_readfirstlane(__builtin_bit_cast(int, exp2f(-(float)(h + 1)) * LOG2E)));
; #pragma unroll
;     for (int j = 0; j < 2; ++j)
; #pragma unroll
;         for (int ks = 0; ks < 2; ++ks) { const u32x4 qv = __builtin_bit_cast(u32x4, qf[j][ks]); u32x4 o;
;             o.x = pk2(bflo(qv.x) * sc, bfhi(qv.x) * sc); o.y = pk2(bflo(qv.y) * sc, bfhi(qv.y) * sc); o.z = pk2(bflo(qv.z) * sc, bfhi(qv.z) * sc); o.w = pk2(bflo(qv.w) * sc, bfhi(qv.w) * sc);
;             qf[j][ks] = __builtin_bit_cast(bf16x8, o); }
;     float sbias[16];
; #pragma unroll
;     for (int i = 0; i < 16; ++i) sbias[i] = __builtin_bit_cast(float, __builtin_amdgcn_readfirstlane(__builtin_bit_cast(int, sl * (float)(16 * (i >> 2) + (i & 3)))));
; template <int L> DI void layer_phases(const Params& P, Frame& F, const XcdBarrier& bar, int lo, int hi) {
;     ...
;             const float li = (L == 0) ? 0.2f : 0.35550906759f;
;             const float d1 = wave_sum(P.in[I_LQ1][L * 64 + F.lane] * P.in[I_LK1][L * 64 + F.lane]), d2 = wave_sum(P.in[I_LQ2][L * 64 + F.lane] * P.in[I_LK2][L * 64 + F.lane]);
;             const float lam = __expf(d1) - __expf(d2) + li;
;             unsigned* qctr = (unsigned*)(ws + WS_CTL) + CW_QUEUE + 64 * L;
;             for (;;) {
;                 __syncthreads();
;                 if (F.tid == 0) F.MISC[24] = __hip_atomic_fetch_add(qctr, 1u, __ATOMIC_RELAXED, __HIP_MEMORY_SCOPE_AGENT);
;                 __syncthreads();
;                 const int u = (int)F.MISC[24];
;                 if (u >= 1024) break;
.LBB0_1045:
	v_ashrrev_i32_e32 v137, 31, v136
	s_waitcnt lgkmcnt(0)
	v_readlane_b32 s4, v254, 5
	v_lshlrev_b64 v[0:1], 2, v[136:137]
	v_readlane_b32 s6, v254, 7
	v_readlane_b32 s7, v254, 8
	v_readlane_b32 s8, v254, 9
	v_readlane_b32 s9, v254, 10
	v_lshl_add_u64 v[2:3], s[6:7], 0, v[0:1]
	v_readlane_b32 s10, v254, 11
	v_readlane_b32 s11, v254, 12
	v_readlane_b32 s12, v254, 13
	v_readlane_b32 s13, v254, 14
	global_load_dword v4, v[2:3], off
	v_lshl_add_u64 v[2:3], s[8:9], 0, v[0:1]
	global_load_dword v5, v[2:3], off
	v_lshl_add_u64 v[2:3], s[10:11], 0, v[0:1]
	v_lshl_add_u64 v[0:1], s[12:13], 0, v[0:1]
	global_load_dword v2, v[2:3], off
	v_xor_b32_e32 v3, 32, v193
	global_load_dword v1, v[0:1], off
	v_and_b32_e32 v0, 64, v193
	v_add_u32_e32 v12, 64, v0
	v_ashrrev_i32_e32 v6, 4, v136
	v_cmp_lt_i32_e32 vcc, v3, v12
	v_add_u32_e32 v8, 0x200, v138
	v_bfe_u32 v9, v136, 3, 1
	s_movk_i32 s6, 0x2400
	v_bfe_u32 v11, v136, 2, 2
	v_lshlrev_b32_e32 v130, 2, v6
	v_cndmask_b32_e32 v3, v193, v3, vcc
	v_ashrrev_i32_e32 v128, 4, v8
	v_mul_u32_u24_e32 v182, 0x2400, v9
	v_mad_u32_u24 v8, v9, s6, 0
	v_or_b32_e32 v9, v130, v11
	v_lshlrev_b32_e32 v190, 2, v3
	v_lshlrev_b32_e32 v7, 3, v136
	v_ashrrev_i32_e32 v114, 4, v138
	s_movk_i32 s7, 0x90
	s_movk_i32 s8, 0x110
	v_and_b32_e32 v0, 24, v7
	v_mul_lo_u32 v183, v114, s7
	v_mul_lo_u32 v188, v128, s7
	s_add_u32 s0, s54, 0x2000
	s_addc_u32 s1, s55, 0
	v_lshlrev_b32_e32 v10, 4, v136
	s_add_u32 s58, s54, 0x41600000
	v_and_b32_e32 v127, 15, v136
	v_lshlrev_b32_e32 v124, 3, v6
	v_and_b32_e32 v184, 0x70, v10
	v_add_u32_e32 v6, v8, v183
	s_addc_u32 s59, s55, 0
	s_lshl_b32 s64, s86, 4
	v_mul_lo_u32 v185, v114, s8
	v_mul_lo_u32 v189, v128, s8
	v_sub_u32_e32 v10, v130, v127
	v_readlane_b32 s5, v254, 6
	v_readlane_b32 s14, v254, 15
	v_readlane_b32 s15, v254, 16
	v_and_b32_e32 v126, 0x78, v7
	v_lshlrev_b32_e32 v186, 4, v127
	v_add_u32_e32 v7, 0, v185
	v_ashrrev_i32_e32 v131, 31, v130
	s_mov_b32 s39, 0
	v_cmp_eq_u32_e64 s[4:5], 0, v138
	v_mov_b32_e32 v113, 0
	v_and_b32_e32 v161, -16, v136
	s_movk_i32 s3, 0x3800
	s_mov_b32 s56, 0x3e38aa3b
	s_movk_i32 s33, 0x2000
	s_mov_b32 s57, 0xff800000
	v_mov_b32_e32 v179, 0x358637bd
	v_mov_b32_e32 v180, 0x42800000
	v_mov_b32_e32 v181, 0x3fb8aa3b
	v_mov_b32_e32 v116, 2.0
	v_mov_b32_e32 v117, 0x40400000
	v_mov_b32_e32 v118, 0x41800000
	v_mov_b32_e32 v119, 0x41880000
	v_mov_b32_e32 v120, 0x41900000
	v_mov_b32_e32 v121, 0x41980000
	v_mov_b32_e32 v122, 0x42000000
	v_mov_b32_e32 v123, 0x42040000
	v_ashrrev_i32_e32 v115, 31, v114
	v_mul_u32_u24_e32 v187, 0x90, v127
	v_ashrrev_i32_e32 v125, 31, v124
	v_ashrrev_i32_e32 v129, 31, v128
	v_lshl_add_u64 v[134:135], v[130:131], 2, s[14:15]
	s_add_i32 s65, 0, 0x22060
	v_add_u32_e32 v191, v7, v186
	v_mov_b32_e32 v136, 0x42080000
	v_mov_b32_e32 v137, 0x420c0000
	v_mov_b32_e32 v138, 0x42400000
	v_mov_b32_e32 v139, 0x42440000
	v_mov_b32_e32 v140, 0x42480000
	v_mov_b32_e32 v141, 0x424c0000
	s_waitcnt vmcnt(2)
	v_mul_f32_e32 v3, v4, v5
	v_mov_b32_e32 v198, 0xff800000
	v_readlane_b32 s16, v254, 17
	v_mov_b32_dpp v3, v3 quad_perm:[1,0,3,2] row_mask:0xf bank_mask:0xf bound_ctrl:1
	v_fmac_f32_e32 v3, v4, v5
	s_waitcnt vmcnt(0)
	v_mul_f32_e32 v11, v2, v1
	v_add_u32_e32 v5, v8, v188
	v_add_u32_e32 v8, 0, v189
	v_mov_b32_dpp v11, v11 quad_perm:[1,0,3,2] row_mask:0xf bank_mask:0xf bound_ctrl:1
	v_fmac_f32_e32 v11, v2, v1
	v_add_f32_dpp v1, v3, v3 quad_perm:[2,3,0,1] row_mask:0xf bank_mask:0xf bound_ctrl:1
	ds_swizzle_b32 v3, v1 offset:swizzle(SWAP,4)
	v_add_f32_dpp v2, v11, v11 quad_perm:[2,3,0,1] row_mask:0xf bank_mask:0xf bound_ctrl:1
	ds_swizzle_b32 v4, v2 offset:swizzle(SWAP,4)
	v_add_u32_e32 v193, v5, v184
	v_add_u32_e32 v194, v8, v186
	s_waitcnt lgkmcnt(1)
	v_add_f32_e32 v1, v1, v3
	ds_swizzle_b32 v3, v1 offset:swizzle(SWAP,8)
	s_waitcnt lgkmcnt(1)
	v_add_f32_e32 v2, v2, v4
	ds_swizzle_b32 v4, v2 offset:swizzle(SWAP,8)
	v_mad_u64_u32 v[132:133], s[6:7], v9, s8, v[0:1]
	s_waitcnt lgkmcnt(1)
	v_add_f32_e32 v0, v1, v3
	v_add_u32_e32 v133, v6, v184
	s_waitcnt lgkmcnt(0)
	v_add_f32_e32 v1, v2, v4
	ds_swizzle_b32 v2, v0 offset:swizzle(SWAP,16)
	ds_swizzle_b32 v3, v1 offset:swizzle(SWAP,16)
	v_or_b32_e32 v6, s64, v127
	v_subrev_u32_e32 v4, s64, v10
	v_add_u32_e32 v195, 64, v4
	s_waitcnt lgkmcnt(1)
	v_add_f32_e32 v0, v0, v2
	s_waitcnt lgkmcnt(0)
	v_add_f32_e32 v1, v1, v3
	ds_bpermute_b32 v2, v190, v0
	ds_bpermute_b32 v3, v190, v1
	v_readlane_b32 s17, v254, 18
	v_readlane_b32 s18, v254, 19
	v_readlane_b32 s19, v254, 20
	s_waitcnt lgkmcnt(1)
	v_add_f32_e32 v0, v0, v2
	s_waitcnt lgkmcnt(0)
	v_add_f32_e32 v1, v1, v3
	v_mul_f32_e32 v0, 0x3fb8aa3b, v0
	v_mul_f32_e32 v1, 0x3fb8aa3b, v1
	v_exp_f32_e32 v0, v0
	v_exp_f32_e32 v1, v1
	v_sub_u32_e32 v2, v6, v130
	v_subrev_u32_e32 v196, 64, v2
	v_sub_f32_e32 v0, v0, v1
	v_add_f32_e32 v197, 0x3e4ccccd, v0
	s_mov_b64 s[6:7], exec
	s_and_b64 exec, exec, s[4:5]
	v_mov_b32_e32 v252, 1
	global_atomic_add v252, v113, v252, s[0:1] sc0
	s_mov_b64 exec, s[6:7]
	s_cmp_lt_u32 s86, 4
	s_cbranch_scc1 .Lprio_a_done
	s_setprio 1
.Lprio_a_done:
	s_branch .LBB0_1048

; __device__ __forceinline__ unsigned xb_add(unsigned* p, unsigned v) { return __hip_atomic_fetch_add(p, v, __ATOMIC_RELAXED, __HIP_MEMORY_SCOPE_AGENT); }
; __device__ __forceinline__ void xcd_barrier(const XcdBarrier& b) {
;     asm volatile("s_waitcnt vmcnt(0)" ::: "memory");
;     __syncthreads();
;     if (threadIdx.x == 0) {
;         unsigned* bar = b.bar;
;         __builtin_amdgcn_s_waitcnt(0);
;         unsigned nloc = b.st[0], nx = b.st[1];
;         if (nloc == 0u) { xcd_barrier_complete(bar, b.x, nloc, nx); b.st[0] = nloc; b.st[1] = nx; }
;         const unsigned old = xb_add(&bar[XB_XSUB(b.x)], 1u);
; template <int L> DI void layer_phases(const Params& P, Frame& F, const XcdBarrier& bar, int lo, int hi) {
;     ...
;             for (;;) {
;                 __syncthreads();
;                 if (F.tid == 0) F.MISC[24] = __hip_atomic_fetch_add(qctr, 1u, __ATOMIC_RELAXED, __HIP_MEMORY_SCOPE_AGENT);
;                 __syncthreads();
;                 const int u = (int)F.MISC[24];
;                 if (u >= 1024) break;
;                 const int bh = u & 63; attn_block(P, F, L, bh >> 3, bh & 7, 15 - (u >> 6), lam, 1.0f - li); } }
.LBB0_1070:
	s_setprio 0
	v_readlane_b32 s64, v254, 57
	v_readlane_b32 s65, v254, 58
	s_cmp_lt_i32 s65, 7
	s_cbranch_scc1 .LBB0_1124
	s_waitcnt vmcnt(0)
	s_barrier
	s_mov_b64 s[0:1], exec
	v_readlane_b32 s4, v254, 3
	v_readlane_b32 s5, v254, 4
	s_and_b64 s[4:5], s[0:1], s[4:5]
	s_mov_b64 exec, s[4:5]
	s_cbranch_execz .LBB0_1123
	s_add_i32 s3, 0, 0x22020
	v_mov_b32_e32 v0, s3
	s_waitcnt vmcnt(0) expcnt(0) lgkmcnt(0)
	ds_read_b32 v2, v0
	s_add_i32 s3, 0, 0x22024
	v_mov_b32_e32 v0, s3
	ds_read_b32 v0, v0
	s_waitcnt lgkmcnt(1)
	v_cmp_ne_u32_e32 vcc, 0, v2
	s_cbranch_vccnz .LBB0_1087
	v_readlane_b32 s4, v254, 53
	v_readlane_b32 s5, v254, 54
	s_load_dwordx2 s[8:9], s[4:5], 0x108
	s_load_dword s3, s[4:5], 0x110
	s_add_u32 s4, s54, 0x4200
	s_addc_u32 s5, s55, 0
	s_add_u32 s6, s54, 0x4400
	s_waitcnt lgkmcnt(0)
	s_mul_i32 s7, s9, s8
	s_mul_i32 s3, s7, s3
	s_addc_u32 s7, s55, 0
	s_add_u32 s8, s54, 0x4500
	s_addc_u32 s9, s55, 0
	s_add_u32 s10, s54, 0x4600
	s_addc_u32 s11, s55, 0
	s_add_u32 s12, s54, 0x4700
	s_addc_u32 s13, s55, 0
	s_add_u32 s14, s54, 0x4800
	s_addc_u32 s15, s55, 0
	s_add_u32 s16, s54, 0x4900
	s_addc_u32 s17, s55, 0
	s_add_u32 s18, s54, 0x4a00
	s_addc_u32 s19, s55, 0
	s_add_u32 s20, s54, 0x4b00
	s_addc_u32 s21, s55, 0
	s_add_u32 s22, s54, 0x4c00
	s_addc_u32 s23, s55, 0
	s_add_u32 s24, s54, 0x4d00
	s_addc_u32 s25, s55, 0
	s_add_u32 s26, s54, 0x4e00
	s_addc_u32 s27, s55, 0
	s_add_u32 s28, s54, 0x4f00
	s_addc_u32 s29, s55, 0
	s_add_u32 s30, s54, 0x5000
	s_addc_u32 s31, s55, 0
	s_add_u32 s34, s54, 0x5100
	s_addc_u32 s35, s55, 0
	s_add_u32 s36, s54, 0x5200
	s_addc_u32 s37, s55, 0
	s_add_u32 s38, s54, 0x5300
	s_addc_u32 s39, s55, 0
	s_mov_b32 s33, 1
	v_mov_b32_e32 v16, 0
	s_branch .LBB0_1075

; DI unsigned pk2(float lo, float hi) { const f32x2 v = {lo, hi}; return __builtin_bit_cast(unsigned, __builtin_convertvector(v, bf16x2_t)); }
; DI void attn_block(const Params& P, const Frame& F, int L, int b, int h, int qb, float lam, float oml) {
;     ...
;     const int lane = F.lane, c = lane & 15, rq = lane >> 4, wave = F.wave;
;     const int q0 = qb * 128, qrow = q0 + 16 * wave + c;
;     const size_t rowbase = (size_t)b * SEQ;
;     bf16x8 qf[2][2];
; #pragma unroll
;     for (int j = 0; j < 2; ++j)
; #pragma unroll
;         for (int ks = 0; ks < 2; ++ks) qf[j][ks] = *(const bf16x8*)(Z + (rowbase + qrow) * NZ + 3072 + h * 128 + j * 64 + 32 * ks + 8 * rq);
;     const float LOG2E = 1.4426950408889634f;
;     const float sc = 0.125f * LOG2E, sl = __builtin_bit_cast(float, __builtin_amdgcn_readfirstlane(__builtin_bit_cast(int, exp2f(-(float)(h + 1)) * LOG2E)));
; #pragma unroll
;     for (int j = 0; j < 2; ++j)
; #pragma unroll
;         for (int ks = 0; ks < 2; ++ks) { const u32x4 qv = __builtin_bit_cast(u32x4, qf[j][ks]); u32x4 o;
;             o.x = pk2(bflo(qv.x) * sc, bfhi(qv.x) * sc); o.y = pk2(bflo(qv.y) * sc, bfhi(qv.y) * sc); o.z = pk2(bflo(qv.z) * sc, bfhi(qv.z) * sc); o.w = pk2(bflo(qv.w) * sc, bfhi(qv.w) * sc);
;             qf[j][ks] = __builtin_bit_cast(bf16x8, o); }
;     float sbias[16];
; #pragma unroll
;     for (int i = 0; i < 16; ++i) sbias[i] = __builtin_bit_cast(float, __builtin_amdgcn_readfirstlane(__builtin_bit_cast(int, sl * (float)(16 * (i >> 2) + (i & 3)))));
; template <int L> DI void layer_phases(const Params& P, Frame& F, const XcdBarrier& bar, int lo, int hi) {
;     ...
;             const float li = (L == 0) ? 0.2f : 0.35550906759f;
;             const float d1 = wave_sum(P.in[I_LQ1][L * 64 + F.lane] * P.in[I_LK1][L * 64 + F.lane]), d2 = wave_sum(P.in[I_LQ2][L * 64 + F.lane] * P.in[I_LK2][L * 64 + F.lane]);
;             const float lam = __expf(d1) - __expf(d2) + li;
;             unsigned* qctr = (unsigned*)(ws + WS_CTL) + CW_QUEUE + 64 * L;
;             for (;;) {
;                 __syncthreads();
;                 if (F.tid == 0) F.MISC[24] = __hip_atomic_fetch_add(qctr, 1u, __ATOMIC_RELAXED, __HIP_MEMORY_SCOPE_AGENT);
;                 __syncthreads();
;                 const int u = (int)F.MISC[24];
;                 if (u >= 1024) break;
.LBB0_2610:
	v_ashrrev_i32_e32 v113, 31, v112
	v_readlane_b32 s4, v254, 5
	v_lshlrev_b64 v[0:1], 2, v[112:113]
	v_readlane_b32 s6, v254, 7
	v_readlane_b32 s7, v254, 8
	v_readlane_b32 s8, v254, 9
	v_readlane_b32 s9, v254, 10
	v_lshl_add_u64 v[2:3], s[6:7], 0, v[0:1]
	v_readlane_b32 s10, v254, 11
	v_readlane_b32 s11, v254, 12
	v_readlane_b32 s12, v254, 13
	v_readlane_b32 s13, v254, 14
	global_load_dword v4, v[2:3], off offset:256
	v_lshl_add_u64 v[2:3], s[8:9], 0, v[0:1]
	global_load_dword v5, v[2:3], off offset:256
	v_lshl_add_u64 v[2:3], s[10:11], 0, v[0:1]
	v_lshl_add_u64 v[0:1], s[12:13], 0, v[0:1]
	global_load_dword v2, v[2:3], off offset:256
	v_xor_b32_e32 v3, 32, v154
	global_load_dword v1, v[0:1], off offset:256
	v_and_b32_e32 v0, 64, v154
	v_add_u32_e32 v12, 64, v0
	v_ashrrev_i32_e32 v6, 4, v112
	v_cmp_lt_i32_e32 vcc, v3, v12
	v_add_u32_e32 v8, 0x200, v114
	v_bfe_u32 v9, v112, 3, 1
	s_movk_i32 s6, 0x2400
	v_bfe_u32 v11, v112, 2, 2
	v_lshlrev_b32_e32 v106, 2, v6
	v_cndmask_b32_e32 v3, v154, v3, vcc
	v_ashrrev_i32_e32 v104, 4, v8
	v_mul_u32_u24_e32 v182, 0x2400, v9
	v_mad_u32_u24 v8, v9, s6, 0
	v_or_b32_e32 v9, v106, v11
	v_lshlrev_b32_e32 v190, 2, v3
	v_lshlrev_b32_e32 v7, 3, v112
	v_ashrrev_i32_e32 v98, 4, v114
	s_movk_i32 s7, 0x90
	s_movk_i32 s8, 0x110
	v_and_b32_e32 v0, 24, v7
	v_mul_lo_u32 v183, v98, s7
	v_mul_lo_u32 v188, v104, s7
	s_add_u32 s0, s54, 0x2100
	s_addc_u32 s1, s55, 0
	v_lshlrev_b32_e32 v10, 4, v112
	s_add_u32 s56, s54, 0x41600000
	v_and_b32_e32 v103, 15, v112
	v_lshlrev_b32_e32 v100, 3, v6
	v_and_b32_e32 v184, 0x70, v10
	v_add_u32_e32 v6, v8, v183
	s_addc_u32 s57, s55, 0
	s_lshl_b32 s66, s86, 4
	v_mul_lo_u32 v185, v98, s8
	v_mul_lo_u32 v189, v104, s8
	v_sub_u32_e32 v10, v106, v103
	v_readlane_b32 s5, v254, 6
	v_readlane_b32 s14, v254, 15
	v_readlane_b32 s15, v254, 16
	v_and_b32_e32 v102, 0x78, v7
	v_lshlrev_b32_e32 v186, 4, v103
	v_add_u32_e32 v7, 0, v185
	v_ashrrev_i32_e32 v107, 31, v106
	s_mov_b32 s41, 0
	v_cmp_eq_u32_e64 s[4:5], 0, v114
	v_mov_b32_e32 v97, 0
	v_and_b32_e32 v145, -16, v112
	s_movk_i32 s3, 0x3ff
	s_movk_i32 s33, 0x3800
	s_mov_b64 s[42:43], 0x1800
	s_movk_i32 s47, 0x1000
	s_mov_b32 s62, 0x42fc0000
	s_mov_b32 s46, 0x3e38aa3b
	s_movk_i32 s63, 0x2000
	s_mov_b32 s64, 0xff800000
	v_mov_b32_e32 v163, 0x358637bd
	s_mov_b64 s[48:49], 0x61400400
	s_mov_b32 s65, 0x61400000
	v_mov_b32_e32 v180, 0x42800000
	v_mov_b32_e32 v181, 0x3fb8aa3b
	v_ashrrev_i32_e32 v99, 31, v98
	v_mul_u32_u24_e32 v187, 0x90, v103
	v_ashrrev_i32_e32 v101, 31, v100
	v_ashrrev_i32_e32 v105, 31, v104
	v_lshl_add_u64 v[110:111], v[106:107], 2, s[14:15]
	s_add_i32 s67, 0, 0x22060
	v_add_u32_e32 v191, v7, v186
	v_mov_b32_e32 v112, 2.0
	v_mov_b32_e32 v113, 0x40400000
	v_mov_b32_e32 v114, 0x41800000
	v_mov_b32_e32 v115, 0x41880000
	v_mov_b32_e32 v116, 0x41900000
	v_mov_b32_e32 v117, 0x41980000
	v_mov_b32_e32 v118, 0x42000000
	v_mov_b32_e32 v119, 0x42040000
	s_waitcnt vmcnt(2)
	v_mul_f32_e32 v3, v4, v5
	v_mov_b32_e32 v120, 0x42080000
	v_mov_b32_e32 v121, 0x420c0000
	v_mov_b32_dpp v3, v3 quad_perm:[1,0,3,2] row_mask:0xf bank_mask:0xf bound_ctrl:1
	v_fmac_f32_e32 v3, v4, v5
	s_waitcnt vmcnt(0)
	v_mul_f32_e32 v11, v2, v1
	v_add_u32_e32 v5, v8, v188
	v_add_u32_e32 v8, 0, v189
	v_mov_b32_dpp v11, v11 quad_perm:[1,0,3,2] row_mask:0xf bank_mask:0xf bound_ctrl:1
	v_fmac_f32_e32 v11, v2, v1
	v_add_f32_dpp v1, v3, v3 quad_perm:[2,3,0,1] row_mask:0xf bank_mask:0xf bound_ctrl:1
	ds_swizzle_b32 v3, v1 offset:swizzle(SWAP,4)
	v_add_f32_dpp v2, v11, v11 quad_perm:[2,3,0,1] row_mask:0xf bank_mask:0xf bound_ctrl:1
	ds_swizzle_b32 v4, v2 offset:swizzle(SWAP,4)
	v_add_u32_e32 v193, v5, v184
	v_add_u32_e32 v194, v8, v186
	s_waitcnt lgkmcnt(1)
	v_add_f32_e32 v1, v1, v3
	ds_swizzle_b32 v3, v1 offset:swizzle(SWAP,8)
	s_waitcnt lgkmcnt(1)
	v_add_f32_e32 v2, v2, v4
	ds_swizzle_b32 v4, v2 offset:swizzle(SWAP,8)
	v_mad_u64_u32 v[108:109], s[6:7], v9, s8, v[0:1]
	s_waitcnt lgkmcnt(1)
	v_add_f32_e32 v0, v1, v3
	v_add_u32_e32 v109, v6, v184
	s_waitcnt lgkmcnt(0)
	v_add_f32_e32 v1, v2, v4
	ds_swizzle_b32 v2, v0 offset:swizzle(SWAP,16)
	ds_swizzle_b32 v3, v1 offset:swizzle(SWAP,16)
	v_or_b32_e32 v6, s66, v103
	v_subrev_u32_e32 v4, s66, v10
	v_add_u32_e32 v195, 64, v4
	s_waitcnt lgkmcnt(1)
	v_add_f32_e32 v0, v0, v2
	s_waitcnt lgkmcnt(0)
	v_add_f32_e32 v1, v1, v3
	ds_bpermute_b32 v2, v190, v0
	ds_bpermute_b32 v3, v190, v1
	v_mov_b32_e32 v122, 0x42400000
	v_mov_b32_e32 v123, 0x42440000
	v_mov_b32_e32 v124, 0x42480000
	s_waitcnt lgkmcnt(1)
	v_add_f32_e32 v0, v0, v2
	s_waitcnt lgkmcnt(0)
	v_add_f32_e32 v1, v1, v3
	v_mul_f32_e32 v0, 0x3fb8aa3b, v0
	v_mul_f32_e32 v1, 0x3fb8aa3b, v1
	v_exp_f32_e32 v0, v0
	v_exp_f32_e32 v1, v1
	v_sub_u32_e32 v2, v6, v106
	v_subrev_u32_e32 v196, 64, v2
	v_mov_b32_e32 v125, 0x424c0000
	v_sub_f32_e32 v0, v0, v1
	v_add_f32_e32 v197, 0x3eb60549, v0
	v_mov_b32_e32 v198, 0xff800000
	v_readlane_b32 s16, v254, 17
	v_readlane_b32 s17, v254, 18
	v_readlane_b32 s18, v254, 19
	v_readlane_b32 s19, v254, 20
	s_mov_b64 s[6:7], exec
	s_and_b64 exec, exec, s[4:5]
	v_mov_b32_e32 v252, 1
	global_atomic_add v252, v97, v252, s[0:1] sc0
	s_mov_b64 exec, s[6:7]
	s_cmp_lt_u32 s86, 4
	s_cbranch_scc1 .Lprio_b_done
	s_setprio 1

; __device__ __forceinline__ unsigned xb_add(unsigned* p, unsigned v) { return __hip_atomic_fetch_add(p, v, __ATOMIC_RELAXED, __HIP_MEMORY_SCOPE_AGENT); }
; __device__ __forceinline__ void xcd_barrier(const XcdBarrier& b) {
;     asm volatile("s_waitcnt vmcnt(0)" ::: "memory");
;     __syncthreads();
;     if (threadIdx.x == 0) {
;         unsigned* bar = b.bar;
;         __builtin_amdgcn_s_waitcnt(0);
;         unsigned nloc = b.st[0], nx = b.st[1];
;         if (nloc == 0u) { xcd_barrier_complete(bar, b.x, nloc, nx); b.st[0] = nloc; b.st[1] = nx; }
;         const unsigned old = xb_add(&bar[XB_XSUB(b.x)], 1u);
; template <int L> DI void layer_phases(const Params& P, Frame& F, const XcdBarrier& bar, int lo, int hi) {
;     ...
;             for (;;) {
;                 __syncthreads();
;                 if (F.tid == 0) F.MISC[24] = __hip_atomic_fetch_add(qctr, 1u, __ATOMIC_RELAXED, __HIP_MEMORY_SCOPE_AGENT);
;                 __syncthreads();
;                 const int u = (int)F.MISC[24];
;                 if (u >= 1024) break;
;                 const int bh = u & 63; attn_block(P, F, L, bh >> 3, bh & 7, 15 - (u >> 6), lam, 1.0f - li); } }
.LBB0_2635:
	s_setprio 0
	v_readlane_b32 s64, v254, 57
	v_readlane_b32 s65, v254, 58
	s_cmp_lt_i32 s65, 20
	s_cbranch_scc1 .LBB0_2689
	s_waitcnt vmcnt(0)
	s_barrier
	s_mov_b64 s[0:1], exec
	v_readlane_b32 s4, v254, 3
	v_readlane_b32 s5, v254, 4
	s_and_b64 s[4:5], s[0:1], s[4:5]
	s_mov_b64 exec, s[4:5]
	s_cbranch_execz .LBB0_2688
	s_add_i32 s3, 0, 0x22020
	v_mov_b32_e32 v0, s3
	s_waitcnt vmcnt(0) expcnt(0) lgkmcnt(0)
	ds_read_b32 v2, v0
	s_add_i32 s3, 0, 0x22024
	v_mov_b32_e32 v0, s3
	ds_read_b32 v0, v0
	s_waitcnt lgkmcnt(1)
	v_cmp_ne_u32_e32 vcc, 0, v2
	s_cbranch_vccnz .LBB0_2652
	v_readlane_b32 s4, v254, 53
	v_readlane_b32 s5, v254, 54
	s_load_dwordx2 s[8:9], s[4:5], 0x108
	s_load_dword s3, s[4:5], 0x110
	s_add_u32 s4, s54, 0x4200
	s_addc_u32 s5, s55, 0
	s_add_u32 s6, s54, 0x4400
	s_waitcnt lgkmcnt(0)
	s_mul_i32 s7, s9, s8
	s_mul_i32 s3, s7, s3
	s_addc_u32 s7, s55, 0
	s_add_u32 s8, s54, 0x4500
	s_addc_u32 s9, s55, 0
	s_add_u32 s10, s54, 0x4600
	s_addc_u32 s11, s55, 0
	s_add_u32 s12, s54, 0x4700
	s_addc_u32 s13, s55, 0
	s_add_u32 s14, s54, 0x4800
	s_addc_u32 s15, s55, 0
	s_add_u32 s16, s54, 0x4900
	s_addc_u32 s17, s55, 0
	s_add_u32 s18, s54, 0x4a00
	s_addc_u32 s19, s55, 0
	s_add_u32 s20, s54, 0x4b00
	s_addc_u32 s21, s55, 0
	s_add_u32 s22, s54, 0x4c00
	s_addc_u32 s23, s55, 0
	s_add_u32 s24, s54, 0x4d00
	s_addc_u32 s25, s55, 0
	s_add_u32 s26, s54, 0x4e00
	s_addc_u32 s27, s55, 0
	s_add_u32 s28, s54, 0x4f00
	s_addc_u32 s29, s55, 0
	s_add_u32 s30, s54, 0x5000
	s_addc_u32 s31, s55, 0
	s_add_u32 s34, s54, 0x5100
	s_addc_u32 s35, s55, 0
	s_add_u32 s36, s54, 0x5200
	s_addc_u32 s37, s55, 0
	s_add_u32 s40, s54, 0x5300
	s_addc_u32 s41, s55, 0
	s_mov_b32 s33, 1
	v_mov_b32_e32 v16, 0
	s_branch .LBB0_2640
